# peeled first K-loop iteration with SrcC=0 (no 128 v_mov accumulator zeroing per unit) in gate-up and residual GEMMs; dropped compiler vmcnt(0) before the gate-up unit loop
# speedup vs baseline: 1.0059x; 1.0031x over previous
; #define PG8_STAGE(bufoff, gbase, voff) do { _Pragma("unroll") for (int _i = 0; _i < 2; ++_i) \
;         __builtin_amdgcn_global_load_lds((const unsigned*)((const char*)(gbase) + (voff)[_i]), (PG8_LAS unsigned*)(lds + (bufoff) + ldsw + _i * 8192), 16, 0, 0); } while (0)
; #define PG8_WAIT_V(n) asm volatile("s_waitcnt vmcnt(" #n ")" ::: "memory")
; #define PG8_BAR __builtin_amdgcn_s_barrier()
; template <class Epi, class Sched, bool ALIGN_EPI>
; __device__ __forceinline__ void gemm_phase(PG8_LAS unsigned char* lds, const Gemm g, const Sched& S, const Epi& E, const int tid) {
;     const int wid = __builtin_amdgcn_readfirstlane(tid >> 6), lane = tid & 63, wr = wid >> 2, wc = wid & 3, fr = lane & 15, fq = lane >> 4;
;     const int K = g.K, nt = K / BK, lda = g.lda;
;     unsigned voffA[2], voffB[2];
; #pragma unroll
;     for (int i = 0; i < 2; ++i) { int R, C; stage_rc(tid * 16 + i * 8192, R, C); const int Rb = Epi::PERM ? ((R & ~31) + perm32(R & 31)) : R;
;         voffA[i] = (unsigned)(R * (g.ta ? BK : lda) + C) * 2u; voffB[i] = (unsigned)(Rb * (g.tb ? BK : K) + C) * 2u; }
;     const size_t kstepA = g.ta ? (size_t)BM * BK * 2 : (size_t)(BK * 2), kstepB = g.tb ? (size_t)BM * BK * 2 : (size_t)(BK * 2);
;     const size_t hstepA = g.ta ? (size_t)HALF * BK * 2 : (size_t)HALF * lda * 2, hstepB = g.tb ? (size_t)HALF * BK * 2 : (size_t)HALF * K * 2;
;     const size_t tstepA = g.ta ? (size_t)(K / BK) * BM * BK * 2 : 2 * hstepA, tstepB = g.tb ? (size_t)(K / BK) * BM * BK * 2 : 2 * hstepB;
;     const unsigned ldsw = (unsigned)wid * 1024u;
;     const int aoff = lds_byte(wr * 64 + fr, fq * 8), boff = lds_byte(wc * 32 + fr, fq * 8);
;     ...
;     const char* cA = (const char*)g.A + (size_t)cur.pm * tstepA + PG8_ACOL(cur); const char* cB = (const char*)g.Bt + (size_t)cur.pn * tstepB;
;     S.a_ready(cur);
;     PG8_STAGE(PG8_SB(0, 0), cB, voffB); PG8_STAGE(PG8_SB(0, 1), cB + hstepB, voffB); PG8_STAGE(PG8_SA(0, 0), cA, voffA); PG8_STAGE(PG8_SA(0, 1), cA + hstepA, voffA);
;     if (wr == 1) PG8_BAR;
;     PG8_WAIT_V(2); PG8_BAR;
;     PG8_STAGE(PG8_SB(1, 0), cB + kstepB, voffB); PG8_STAGE(PG8_SA(1, 0), cA + kstepA, voffA); PG8_STAGE(PG8_SB(1, 1), cB + hstepB + kstepB, voffB);
;     PG8_WAIT_V(6); PG8_BAR;
.LBB0_240:
	v_readlane_b32 s8, v252, 43
	v_readlane_b32 s9, v252, 44
	s_add_u32 s8, s8, 0x2cb5c000
	s_addc_u32 s9, s9, 0
	s_lshl_b32 s3, s3, 5
	s_and_b32 s50, s3, 0x60
	s_lshl_b32 s49, s6, 6
	s_lshl_b32 s10, s6, 13
	s_lshl_b32 s11, s50, 7
	s_add_u32 s6, s18, 0x8000
	v_mov_b32_e32 v151, v129
	s_addc_u32 s7, s19, 0
	s_add_i32 m0, s45, 0x18000
	v_lshl_add_u64 v[8:9], s[6:7], 0, v[150:151]
	v_mov_b32_e32 v147, v129
	s_waitcnt vmcnt(2)
	s_barrier
	global_load_lds_dwordx4 v[8:9], off
	s_add_i32 m0, s45, 0x1a000
	v_lshl_add_u64 v[8:9], s[6:7], 0, v[146:147]
	s_add_u32 s6, s16, 0x8000
	v_mov_b32_e32 v153, v129
	s_addc_u32 s7, s17, 0
	s_add_i32 s51, s45, 0x8000
	v_mov_b32_e32 v149, v129
	global_load_lds_dwordx4 v[8:9], off
	v_lshl_add_u64 v[8:9], s[6:7], 0, v[152:153]
	s_mov_b32 m0, s51
	s_add_i32 s52, s45, 0xa000
	global_load_lds_dwordx4 v[8:9], off
	v_lshl_add_u64 v[8:9], s[6:7], 0, v[148:149]
	s_add_u32 s6, s18, 0xc000
	s_mov_b32 m0, s52
	s_addc_u32 s7, s19, 0
	global_load_lds_dwordx4 v[8:9], off
	s_add_i32 m0, s45, 0x1c000
	v_lshl_add_u64 v[8:9], s[6:7], 0, v[150:151]
	global_load_lds_dwordx4 v[8:9], off
	v_lshl_add_u64 v[8:9], s[6:7], 0, v[146:147]
	s_add_i32 m0, s45, 0x1e000
	v_and_b32_e32 v7, 15, v1
	global_load_lds_dwordx4 v[8:9], off
	v_lshrrev_b32_e32 v8, 1, v1
	v_and_b32_e32 v9, 24, v8
	v_lshlrev_b32_e32 v8, 1, v9
	v_lshlrev_b32_e32 v1, 2, v1
	s_cmpk_lt_u32 s2, 0x100
	v_lshl_or_b32 v8, v7, 6, v8
	v_and_b32_e32 v1, 32, v1
	s_cselect_b64 s[6:7], -1, 0
	s_and_b32 s2, s49, 0xc0
	v_bitop3_b32 v10, v8, s10, v1 bitop3:0xde
	v_bitop3_b32 v178, s11, v8, v1 bitop3:0xf6
	v_or_b32_e32 v1, s2, v7
	v_lshlrev_b32_e32 v128, 7, v1
	v_lshlrev_b32_e32 v1, 10, v5
	v_and_b32_e32 v1, 0xfffff800, v1
	s_add_i32 s53, s49, 0x80
	v_lshl_add_u32 v1, v4, 7, v1
	v_and_b32_e32 v4, 1, v5
	s_and_b32 s2, s53, 0xc0
	v_lshl_or_b32 v1, v4, 6, v1
	v_or_b32_e32 v171, s49, v7
	v_or_b32_e32 v7, s2, v7
	s_lshl_b32 s2, s50, 2
	v_lshl_add_u32 v158, v6, 1, v1
	v_lshlrev_b32_e32 v1, 10, v0
	s_add_i32 s2, s2, 0
	v_and_b32_e32 v1, 0xfffff800, v1
	s_waitcnt vmcnt(6)
	s_add_i32 s2, s2, 0x23800
	v_lshl_add_u32 v1, v2, 7, v1
	v_and_b32_e32 v0, 1, v0
	v_and_or_b32 v8, s3, 32, v9
	v_lshl_add_u32 v179, v9, 2, s2
	v_lshl_add_u64 v[154:155], s[8:9], 0, v[128:129]
	v_lshlrev_b32_e32 v128, 7, v7
	v_lshl_or_b32 v0, v0, 6, v1
	v_readlane_b32 s2, v251, 12
	v_lshl_add_u64 v[156:157], s[8:9], 0, v[128:129]
	v_mov_b32_e32 v159, v129
	v_lshl_add_u32 v160, v3, 1, v0
	v_mov_b32_e32 v161, v129
	s_mov_b32 s56, 0
	v_add_u32_e32 v180, 0, v10
	v_lshlrev_b32_e32 v128, 1, v8
	v_readlane_b32 s57, v251, 11
	s_mov_b32 s55, s2
	s_barrier
	v_readlane_b32 s3, v251, 13
	s_branch .LBB0_243

; #define PG8_STAGE(bufoff, gbase, voff) do { _Pragma("unroll") for (int _i = 0; _i < 2; ++_i) \
;         __builtin_amdgcn_global_load_lds((const unsigned*)((const char*)(gbase) + (voff)[_i]), (PG8_LAS unsigned*)(lds + (bufoff) + ldsw + _i * 8192), 16, 0, 0); } while (0)
; #define PG8_LDA(dst, b, h) do { _Pragma("unroll") for (int m = 0; m < 4; ++m) _Pragma("unroll") for (int k = 0; k < 2; ++k) dst[m][k] = *(const PG8_LAS bf16x8*)(lds + PG8_SA(b, h) + aoff + m * 2048 + k * 1024); } while (0)
; #define PG8_LDB(dst, b, h) do { _Pragma("unroll") for (int n = 0; n < 2; ++n) _Pragma("unroll") for (int k = 0; k < 2; ++k) dst[n][k] = *(const PG8_LAS bf16x8*)(lds + PG8_SB(b, h) + boff + n * 2048 + k * 1024); } while (0)
; #define PG8_WAIT_V(n) asm volatile("s_waitcnt vmcnt(" #n ")" ::: "memory")
; #define PG8_WAIT_L(n) asm volatile("s_waitcnt lgkmcnt(" #n ")" ::: "memory")
; #define PG8_BAR __builtin_amdgcn_s_barrier()
; #define PG8_SCHED __builtin_amdgcn_sched_barrier(0)
; template <class Epi, class Sched, bool ALIGN_EPI>
; __device__ __forceinline__ void gemm_phase(PG8_LAS unsigned char* lds, const Gemm g, const Sched& S, const Epi& E, const int tid) {
;     ...
;         const bool has_next = S.next(ui + 1, nxt);
;         const char* nA = has_next ? (const char*)g.A + (size_t)nxt.pm * tstepA + PG8_ACOL(nxt) : cA; const char* nB = has_next ? (const char*)g.Bt + (size_t)nxt.pn * tstepB : cB;
;         for (int t = 0; t < nt; t += 2) {
;             const bool last = (t == nt - 2);
;             const char* a1 = cA + (size_t)(t + 1) * kstepA;
;             const char* a2 = last ? nA : cA + (size_t)(t + 2) * kstepA; const char* b2 = last ? nB : cB + (size_t)(t + 2) * kstepB;
;             const char* a3 = a2 + kstepA; const char* b3 = b2 + kstepB;
;             if (last && has_next) S.a_ready(nxt);
;             PG8_LDB(B0, 0, 0); PG8_LDB(B1, 0, 1); PG8_SCHED; PG8_LDA(At, 0, 0); PG8_STAGE(PG8_SA(1, 1), a1 + hstepA, voffA);
;             PG8_WAIT_V(8); PG8_WAIT_L(0); PG8_BAR; PG8_MMA(0, 0, At, B0); PG8_MMA(0, 1, At, B1); PG8_BAR; PG8_SCHED;
;             PG8_LDA(At, 0, 1); PG8_STAGE(PG8_SB(0, 0), b2, voffB); PG8_STAGE(PG8_SB(0, 1), b2 + hstepB, voffB); PG8_STAGE(PG8_SA(0, 0), a2, voffA);
;             PG8_WAIT_V(8); PG8_WAIT_L(0); PG8_BAR; PG8_MMA(1, 0, At, B0); PG8_MMA(1, 1, At, B1); PG8_BAR; PG8_SCHED;
.LBB0_245:
	s_ashr_i32 s11, s10, 31
	s_lshl_b64 s[12:13], s[10:11], 20
	s_add_u32 s12, s43, s12
	s_addc_u32 s13, s44, s13
	s_and_b64 s[14:15], s[2:3], exec
	s_cselect_b32 s11, s13, s17
	s_cselect_b32 s58, s12, s16
	s_ashr_i32 s9, s8, 31
	s_lshl_b64 s[14:15], s[8:9], 20
	s_add_u32 s14, s40, s14
	s_addc_u32 s15, s41, s15
	s_and_b64 s[20:21], s[2:3], exec
	s_cselect_b32 s9, s15, s19
	s_cselect_b32 s59, s14, s18
	s_add_u32 s16, s16, 0xc000
	s_addc_u32 s17, s17, 0
	s_add_u32 s60, s18, 0x10000
	s_addc_u32 s61, s19, 0
	s_mov_b32 s62, -2
	v_add_u32_e32 v166, 0x10000, v178
	s_add_u32 s18, s16, 0x4000
	s_addc_u32 s19, s17, 0
	s_cmp_eq_u32 s62, 28
	s_cselect_b32 s22, s58, s18
	s_cselect_b32 s23, s11, s19
	s_cselect_b32 s20, s59, s60
	s_cselect_b32 s21, s9, s61
	s_add_u32 s18, s22, 0x8000
	s_addc_u32 s19, s23, 0
	s_add_i32 s63, 0, 0x10000
	s_add_i32 s66, 0, 0x14000
	ds_read_b128 v[80:83], v166
	ds_read_b128 v[84:87], v166 offset:1024
	ds_read_b128 v[96:99], v166 offset:2048
	ds_read_b128 v[100:103], v166 offset:3072
	ds_read_b128 v[162:165], v166 offset:16384
	ds_read_b128 v[182:185], v166 offset:17408
	ds_read_b128 v[186:189], v166 offset:18432
	ds_read_b128 v[190:193], v166 offset:19456
	s_add_i32 m0, s45, 0xc000
	ds_read_b128 v[194:197], v180
	ds_read_b128 v[198:201], v180 offset:1024
	ds_read_b128 v[202:205], v180 offset:2048
	ds_read_b128 v[206:209], v180 offset:3072
	ds_read_b128 v[210:213], v180 offset:4096
	ds_read_b128 v[214:217], v180 offset:5120
	ds_read_b128 v[218:221], v180 offset:6144
	ds_read_b128 v[222:225], v180 offset:7168
	global_load_lds_dwordx4 v158, s[16:17]
	s_add_i32 m0, s45, 0xe000
	s_nop 0
	global_load_lds_dwordx4 v160, s[16:17]
	s_waitcnt vmcnt(8)
	s_waitcnt lgkmcnt(0)
	s_setprio 1
	s_barrier
	v_mfma_f32_16x16x32_bf16 v[142:145], v[80:83], v[194:197], 0
	v_mfma_f32_16x16x32_bf16 v[134:137], v[96:99], v[194:197], 0
	v_mfma_f32_16x16x32_bf16 v[124:127], v[80:83], v[202:205], 0
	v_mfma_f32_16x16x32_bf16 v[116:119], v[96:99], v[202:205], 0
	v_mfma_f32_16x16x32_bf16 v[108:111], v[80:83], v[210:213], 0
	v_mfma_f32_16x16x32_bf16 v[92:95], v[96:99], v[210:213], 0
	v_mfma_f32_16x16x32_bf16 v[76:79], v[80:83], v[218:221], 0
	v_mfma_f32_16x16x32_bf16 v[68:71], v[96:99], v[218:221], 0
	v_mfma_f32_16x16x32_bf16 v[142:145], v[84:87], v[198:201], v[142:145]
	v_mfma_f32_16x16x32_bf16 v[134:137], v[100:103], v[198:201], v[134:137]
	v_mfma_f32_16x16x32_bf16 v[124:127], v[84:87], v[206:209], v[124:127]
	v_mfma_f32_16x16x32_bf16 v[116:119], v[100:103], v[206:209], v[116:119]
	v_mfma_f32_16x16x32_bf16 v[108:111], v[84:87], v[214:217], v[108:111]
	v_mfma_f32_16x16x32_bf16 v[92:95], v[100:103], v[214:217], v[92:95]
	v_mfma_f32_16x16x32_bf16 v[76:79], v[84:87], v[222:225], v[76:79]
	v_mfma_f32_16x16x32_bf16 v[68:71], v[100:103], v[222:225], v[68:71]
	v_mfma_f32_16x16x32_bf16 v[138:141], v[162:165], v[194:197], 0
	v_mfma_f32_16x16x32_bf16 v[130:133], v[186:189], v[194:197], 0
	v_mfma_f32_16x16x32_bf16 v[120:123], v[162:165], v[202:205], 0
	v_mfma_f32_16x16x32_bf16 v[112:115], v[186:189], v[202:205], 0
	v_mfma_f32_16x16x32_bf16 v[104:107], v[162:165], v[210:213], 0
	v_mfma_f32_16x16x32_bf16 v[88:91], v[186:189], v[210:213], 0
	v_mfma_f32_16x16x32_bf16 v[72:75], v[162:165], v[218:221], 0
	v_mfma_f32_16x16x32_bf16 v[64:67], v[186:189], v[218:221], 0
	v_mfma_f32_16x16x32_bf16 v[138:141], v[182:185], v[198:201], v[138:141]
	v_mfma_f32_16x16x32_bf16 v[130:133], v[190:193], v[198:201], v[130:133]
	v_mfma_f32_16x16x32_bf16 v[120:123], v[182:185], v[206:209], v[120:123]
	v_mfma_f32_16x16x32_bf16 v[112:115], v[190:193], v[206:209], v[112:115]
	v_mfma_f32_16x16x32_bf16 v[104:107], v[182:185], v[214:217], v[104:107]
	v_mfma_f32_16x16x32_bf16 v[88:91], v[190:193], v[214:217], v[88:91]
	v_mfma_f32_16x16x32_bf16 v[72:75], v[182:185], v[222:225], v[72:75]
	v_mfma_f32_16x16x32_bf16 v[64:67], v[190:193], v[222:225], v[64:67]
	s_barrier
	s_setprio 0
	s_add_i32 s63, s63, s42
	s_mov_b32 m0, s63
	ds_read_b128 v[194:197], v180 offset:16384
	ds_read_b128 v[198:201], v180 offset:17408
	ds_read_b128 v[202:205], v180 offset:18432
	ds_read_b128 v[206:209], v180 offset:19456
	ds_read_b128 v[210:213], v180 offset:20480
	ds_read_b128 v[214:217], v180 offset:21504
	ds_read_b128 v[218:221], v180 offset:22528
	ds_read_b128 v[222:225], v180 offset:23552
	global_load_lds_dwordx4 v150, s[20:21]
	s_add_i32 m0, s63, 0x2000
	s_add_u32 s64, s20, 0x4000
	s_addc_u32 s65, s21, 0
	s_add_i32 s63, s66, s42
	global_load_lds_dwordx4 v146, s[20:21]
	s_mov_b32 m0, s63
	s_nop 0
	global_load_lds_dwordx4 v150, s[64:65]
	s_add_i32 m0, s63, 0x2000
	s_nop 0
	global_load_lds_dwordx4 v146, s[64:65]
	s_mov_b32 m0, s45
	s_nop 0
	global_load_lds_dwordx4 v152, s[22:23]
	s_mov_b32 m0, s46
	s_nop 0
	global_load_lds_dwordx4 v148, s[22:23]
	s_waitcnt vmcnt(8)
	s_waitcnt lgkmcnt(0)
	s_setprio 1
	s_barrier
; #define PG8_STAGE(bufoff, gbase, voff) do { _Pragma("unroll") for (int _i = 0; _i < 2; ++_i) \
;         __builtin_amdgcn_global_load_lds((const unsigned*)((const char*)(gbase) + (voff)[_i]), (PG8_LAS unsigned*)(lds + (bufoff) + ldsw + _i * 8192), 16, 0, 0); } while (0)
; #define PG8_LDA(dst, b, h) do { _Pragma("unroll") for (int m = 0; m < 4; ++m) _Pragma("unroll") for (int k = 0; k < 2; ++k) dst[m][k] = *(const PG8_LAS bf16x8*)(lds + PG8_SA(b, h) + aoff + m * 2048 + k * 1024); } while (0)
; #define PG8_LDB(dst, b, h) do { _Pragma("unroll") for (int n = 0; n < 2; ++n) _Pragma("unroll") for (int k = 0; k < 2; ++k) dst[n][k] = *(const PG8_LAS bf16x8*)(lds + PG8_SB(b, h) + boff + n * 2048 + k * 1024); } while (0)
; #define PG8_MMA(ai, bj, At, Bt) do { __builtin_amdgcn_s_setprio(1); _Pragma("unroll") for (int m = 0; m < 4; ++m) _Pragma("unroll") for (int n = 0; n < 2; ++n) _Pragma("unroll") for (int k = 0; k < 2; ++k) \
;         acc[ai][bj][m][n] = __builtin_amdgcn_mfma_f32_16x16x32_bf16(Bt[n][k], At[m][k], acc[ai][bj][m][n], 0, 0, 0); __builtin_amdgcn_s_setprio(0); } while (0)
; #define PG8_WAIT_V(n) asm volatile("s_waitcnt vmcnt(" #n ")" ::: "memory")
; #define PG8_WAIT_L(n) asm volatile("s_waitcnt lgkmcnt(" #n ")" ::: "memory")
; #define PG8_BAR __builtin_amdgcn_s_barrier()
; #define PG8_SCHED __builtin_amdgcn_sched_barrier(0)
; template <class Epi, class Sched, bool ALIGN_EPI>
; __device__ __forceinline__ void gemm_phase(PG8_LAS unsigned char* lds, const Gemm g, const Sched& S, const Epi& E, const int tid) {
;     ...
;             PG8_WAIT_V(8); PG8_WAIT_L(0); PG8_BAR; PG8_MMA(1, 0, At, B0); PG8_MMA(1, 1, At, B1); PG8_BAR; PG8_SCHED;
;             PG8_LDB(B0, 1, 0); PG8_LDB(B1, 1, 1); PG8_SCHED; PG8_LDA(At, 1, 0); PG8_STAGE(PG8_SA(0, 1), a2 + hstepA, voffA);
;             PG8_WAIT_V(8); PG8_WAIT_L(0); PG8_BAR; PG8_MMA(0, 0, At, B0); PG8_MMA(0, 1, At, B1); PG8_BAR; PG8_SCHED;
;             PG8_LDA(At, 1, 1); PG8_STAGE(PG8_SB(1, 0), b3, voffB); PG8_STAGE(PG8_SB(1, 1), b3 + hstepB, voffB); PG8_STAGE(PG8_SA(1, 0), a3, voffA);
	v_mfma_f32_16x16x32_bf16 v[60:63], v[80:83], v[194:197], 0
	v_mfma_f32_16x16x32_bf16 v[52:55], v[96:99], v[194:197], 0
	v_mfma_f32_16x16x32_bf16 v[44:47], v[80:83], v[202:205], 0
	v_mfma_f32_16x16x32_bf16 v[36:39], v[96:99], v[202:205], 0
	v_mfma_f32_16x16x32_bf16 v[28:31], v[80:83], v[210:213], 0
	v_mfma_f32_16x16x32_bf16 v[20:23], v[96:99], v[210:213], 0
	v_mfma_f32_16x16x32_bf16 v[12:15], v[80:83], v[218:221], 0
	v_mfma_f32_16x16x32_bf16 v[4:7], v[96:99], v[218:221], 0
	v_mfma_f32_16x16x32_bf16 v[60:63], v[84:87], v[198:201], v[60:63]
	v_mfma_f32_16x16x32_bf16 v[52:55], v[100:103], v[198:201], v[52:55]
	v_mfma_f32_16x16x32_bf16 v[44:47], v[84:87], v[206:209], v[44:47]
	v_mfma_f32_16x16x32_bf16 v[36:39], v[100:103], v[206:209], v[36:39]
	v_mfma_f32_16x16x32_bf16 v[28:31], v[84:87], v[214:217], v[28:31]
	v_mfma_f32_16x16x32_bf16 v[20:23], v[100:103], v[214:217], v[20:23]
	v_mfma_f32_16x16x32_bf16 v[12:15], v[84:87], v[222:225], v[12:15]
	v_mfma_f32_16x16x32_bf16 v[4:7], v[100:103], v[222:225], v[4:7]
	v_mfma_f32_16x16x32_bf16 v[56:59], v[162:165], v[194:197], 0
	v_mfma_f32_16x16x32_bf16 v[48:51], v[186:189], v[194:197], 0
	v_mfma_f32_16x16x32_bf16 v[40:43], v[162:165], v[202:205], 0
	v_mfma_f32_16x16x32_bf16 v[32:35], v[186:189], v[202:205], 0
	v_mfma_f32_16x16x32_bf16 v[24:27], v[162:165], v[210:213], 0
	v_mfma_f32_16x16x32_bf16 v[16:19], v[186:189], v[210:213], 0
	v_mfma_f32_16x16x32_bf16 v[8:11], v[162:165], v[218:221], 0
	v_mfma_f32_16x16x32_bf16 v[0:3], v[186:189], v[218:221], 0
	v_mfma_f32_16x16x32_bf16 v[56:59], v[182:185], v[198:201], v[56:59]
	v_mfma_f32_16x16x32_bf16 v[48:51], v[190:193], v[198:201], v[48:51]
	v_mfma_f32_16x16x32_bf16 v[40:43], v[182:185], v[206:209], v[40:43]
	v_mfma_f32_16x16x32_bf16 v[32:35], v[190:193], v[206:209], v[32:35]
	v_mfma_f32_16x16x32_bf16 v[24:27], v[182:185], v[214:217], v[24:27]
	v_mfma_f32_16x16x32_bf16 v[16:19], v[190:193], v[214:217], v[16:19]
	v_mfma_f32_16x16x32_bf16 v[8:11], v[182:185], v[222:225], v[8:11]
	v_mfma_f32_16x16x32_bf16 v[0:3], v[190:193], v[222:225], v[0:3]
	s_barrier
	s_setprio 0
	s_add_i32 s63, 0, 0x18000
	s_add_i32 s64, 0, 0x1c000
	ds_read_b128 v[80:83], v166 offset:32768
	ds_read_b128 v[84:87], v166 offset:33792
	ds_read_b128 v[96:99], v166 offset:34816
	ds_read_b128 v[100:103], v166 offset:35840
	ds_read_b128 v[162:165], v166 offset:49152
	ds_read_b128 v[182:185], v166 offset:50176
	ds_read_b128 v[186:189], v166 offset:51200
	ds_read_b128 v[190:193], v166 offset:52224
	s_add_u32 s22, s22, 0x4000
	s_addc_u32 s23, s23, 0
	s_mov_b32 m0, s47
	ds_read_b128 v[194:197], v180 offset:32768
	ds_read_b128 v[198:201], v180 offset:33792
	ds_read_b128 v[202:205], v180 offset:34816
	ds_read_b128 v[206:209], v180 offset:35840
	ds_read_b128 v[210:213], v180 offset:36864
	ds_read_b128 v[214:217], v180 offset:37888
	ds_read_b128 v[218:221], v180 offset:38912
	ds_read_b128 v[222:225], v180 offset:39936
	global_load_lds_dwordx4 v152, s[22:23]
	s_mov_b32 m0, s48
	s_nop 0
	global_load_lds_dwordx4 v148, s[22:23]
	s_waitcnt vmcnt(8)
	s_waitcnt lgkmcnt(0)
	s_setprio 1
	s_barrier
	v_mfma_f32_16x16x32_bf16 v[142:145], v[80:83], v[194:197], v[142:145]
	v_mfma_f32_16x16x32_bf16 v[134:137], v[96:99], v[194:197], v[134:137]
	v_mfma_f32_16x16x32_bf16 v[124:127], v[80:83], v[202:205], v[124:127]
	v_mfma_f32_16x16x32_bf16 v[116:119], v[96:99], v[202:205], v[116:119]
	v_mfma_f32_16x16x32_bf16 v[108:111], v[80:83], v[210:213], v[108:111]
	v_mfma_f32_16x16x32_bf16 v[92:95], v[96:99], v[210:213], v[92:95]
	v_mfma_f32_16x16x32_bf16 v[76:79], v[80:83], v[218:221], v[76:79]
	v_mfma_f32_16x16x32_bf16 v[68:71], v[96:99], v[218:221], v[68:71]
	v_mfma_f32_16x16x32_bf16 v[142:145], v[84:87], v[198:201], v[142:145]
	v_mfma_f32_16x16x32_bf16 v[134:137], v[100:103], v[198:201], v[134:137]
	v_mfma_f32_16x16x32_bf16 v[124:127], v[84:87], v[206:209], v[124:127]
	v_mfma_f32_16x16x32_bf16 v[116:119], v[100:103], v[206:209], v[116:119]
	v_mfma_f32_16x16x32_bf16 v[108:111], v[84:87], v[214:217], v[108:111]
	v_mfma_f32_16x16x32_bf16 v[92:95], v[100:103], v[214:217], v[92:95]
	v_mfma_f32_16x16x32_bf16 v[76:79], v[84:87], v[222:225], v[76:79]
	v_mfma_f32_16x16x32_bf16 v[68:71], v[100:103], v[222:225], v[68:71]
	v_mfma_f32_16x16x32_bf16 v[138:141], v[162:165], v[194:197], v[138:141]
	v_mfma_f32_16x16x32_bf16 v[130:133], v[186:189], v[194:197], v[130:133]
	v_mfma_f32_16x16x32_bf16 v[120:123], v[162:165], v[202:205], v[120:123]
	v_mfma_f32_16x16x32_bf16 v[112:115], v[186:189], v[202:205], v[112:115]
	v_mfma_f32_16x16x32_bf16 v[104:107], v[162:165], v[210:213], v[104:107]
	v_mfma_f32_16x16x32_bf16 v[88:91], v[186:189], v[210:213], v[88:91]
	v_mfma_f32_16x16x32_bf16 v[72:75], v[162:165], v[218:221], v[72:75]
	v_mfma_f32_16x16x32_bf16 v[64:67], v[186:189], v[218:221], v[64:67]
	v_mfma_f32_16x16x32_bf16 v[138:141], v[182:185], v[198:201], v[138:141]
	v_mfma_f32_16x16x32_bf16 v[130:133], v[190:193], v[198:201], v[130:133]
	v_mfma_f32_16x16x32_bf16 v[120:123], v[182:185], v[206:209], v[120:123]
	v_mfma_f32_16x16x32_bf16 v[112:115], v[190:193], v[206:209], v[112:115]
	v_mfma_f32_16x16x32_bf16 v[104:107], v[182:185], v[214:217], v[104:107]
	v_mfma_f32_16x16x32_bf16 v[88:91], v[190:193], v[214:217], v[88:91]
	v_mfma_f32_16x16x32_bf16 v[72:75], v[182:185], v[222:225], v[72:75]
	v_mfma_f32_16x16x32_bf16 v[64:67], v[190:193], v[222:225], v[64:67]
	s_barrier
; #define PG8_STAGE(bufoff, gbase, voff) do { _Pragma("unroll") for (int _i = 0; _i < 2; ++_i) \
;         __builtin_amdgcn_global_load_lds((const unsigned*)((const char*)(gbase) + (voff)[_i]), (PG8_LAS unsigned*)(lds + (bufoff) + ldsw + _i * 8192), 16, 0, 0); } while (0)
; #define PG8_LDA(dst, b, h) do { _Pragma("unroll") for (int m = 0; m < 4; ++m) _Pragma("unroll") for (int k = 0; k < 2; ++k) dst[m][k] = *(const PG8_LAS bf16x8*)(lds + PG8_SA(b, h) + aoff + m * 2048 + k * 1024); } while (0)
; #define PG8_MMA(ai, bj, At, Bt) do { __builtin_amdgcn_s_setprio(1); _Pragma("unroll") for (int m = 0; m < 4; ++m) _Pragma("unroll") for (int n = 0; n < 2; ++n) _Pragma("unroll") for (int k = 0; k < 2; ++k) \
;         acc[ai][bj][m][n] = __builtin_amdgcn_mfma_f32_16x16x32_bf16(Bt[n][k], At[m][k], acc[ai][bj][m][n], 0, 0, 0); __builtin_amdgcn_s_setprio(0); } while (0)
; #define PG8_WAIT_V(n) asm volatile("s_waitcnt vmcnt(" #n ")" ::: "memory")
; #define PG8_WAIT_L(n) asm volatile("s_waitcnt lgkmcnt(" #n ")" ::: "memory")
; #define PG8_BAR __builtin_amdgcn_s_barrier()
; #define PG8_SCHED __builtin_amdgcn_sched_barrier(0)
; template <class Epi, class Sched, bool ALIGN_EPI>
; __device__ __forceinline__ void gemm_phase(PG8_LAS unsigned char* lds, const Gemm g, const Sched& S, const Epi& E, const int tid) {
;     ...
;             PG8_LDA(At, 1, 1); PG8_STAGE(PG8_SB(1, 0), b3, voffB); PG8_STAGE(PG8_SB(1, 1), b3 + hstepB, voffB); PG8_STAGE(PG8_SA(1, 0), a3, voffA);
;             PG8_WAIT_V(8); PG8_WAIT_L(0); PG8_BAR; PG8_MMA(1, 0, At, B0); PG8_MMA(1, 1, At, B1); PG8_BAR; PG8_SCHED;
;         }
	s_setprio 0
	s_add_u32 s22, s20, 0x8000
	s_addc_u32 s23, s21, 0
	s_add_i32 s63, s63, s42
	s_mov_b32 m0, s63
	ds_read_b128 v[194:197], v180 offset:49152
	ds_read_b128 v[198:201], v180 offset:50176
	ds_read_b128 v[202:205], v180 offset:51200
	ds_read_b128 v[206:209], v180 offset:52224
	ds_read_b128 v[210:213], v180 offset:53248
	ds_read_b128 v[214:217], v180 offset:54272
	ds_read_b128 v[218:221], v180 offset:55296
	ds_read_b128 v[222:225], v180 offset:56320
	global_load_lds_dwordx4 v150, s[22:23]
	s_add_i32 m0, s63, 0x2000
	s_add_u32 s20, s20, 0xc000
	s_addc_u32 s21, s21, 0
	global_load_lds_dwordx4 v146, s[22:23]
	s_add_i32 s22, s64, s42
	s_mov_b32 m0, s22
	s_nop 0
	global_load_lds_dwordx4 v150, s[20:21]
	s_add_i32 m0, s22, 0x2000
	s_nop 0
	global_load_lds_dwordx4 v146, s[20:21]
	s_mov_b32 m0, s51
	s_nop 0
	global_load_lds_dwordx4 v152, s[18:19]
	s_mov_b32 m0, s52
	s_nop 0
	global_load_lds_dwordx4 v148, s[18:19]
	s_waitcnt vmcnt(8)
	s_waitcnt lgkmcnt(0)
	s_setprio 1
	s_barrier
	v_mfma_f32_16x16x32_bf16 v[60:63], v[80:83], v[194:197], v[60:63]
	v_mfma_f32_16x16x32_bf16 v[52:55], v[96:99], v[194:197], v[52:55]
	v_mfma_f32_16x16x32_bf16 v[44:47], v[80:83], v[202:205], v[44:47]
	v_mfma_f32_16x16x32_bf16 v[36:39], v[96:99], v[202:205], v[36:39]
	v_mfma_f32_16x16x32_bf16 v[28:31], v[80:83], v[210:213], v[28:31]
	v_mfma_f32_16x16x32_bf16 v[20:23], v[96:99], v[210:213], v[20:23]
	v_mfma_f32_16x16x32_bf16 v[12:15], v[80:83], v[218:221], v[12:15]
	v_mfma_f32_16x16x32_bf16 v[4:7], v[96:99], v[218:221], v[4:7]
	v_mfma_f32_16x16x32_bf16 v[60:63], v[84:87], v[198:201], v[60:63]
	v_mfma_f32_16x16x32_bf16 v[52:55], v[100:103], v[198:201], v[52:55]
	v_mfma_f32_16x16x32_bf16 v[44:47], v[84:87], v[206:209], v[44:47]
	v_mfma_f32_16x16x32_bf16 v[36:39], v[100:103], v[206:209], v[36:39]
	v_mfma_f32_16x16x32_bf16 v[28:31], v[84:87], v[214:217], v[28:31]
	v_mfma_f32_16x16x32_bf16 v[20:23], v[100:103], v[214:217], v[20:23]
	v_mfma_f32_16x16x32_bf16 v[12:15], v[84:87], v[222:225], v[12:15]
	v_mfma_f32_16x16x32_bf16 v[4:7], v[100:103], v[222:225], v[4:7]
	v_mfma_f32_16x16x32_bf16 v[56:59], v[162:165], v[194:197], v[56:59]
	v_mfma_f32_16x16x32_bf16 v[48:51], v[186:189], v[194:197], v[48:51]
	v_mfma_f32_16x16x32_bf16 v[40:43], v[162:165], v[202:205], v[40:43]
	v_mfma_f32_16x16x32_bf16 v[32:35], v[186:189], v[202:205], v[32:35]
	v_mfma_f32_16x16x32_bf16 v[24:27], v[162:165], v[210:213], v[24:27]
	v_mfma_f32_16x16x32_bf16 v[16:19], v[186:189], v[210:213], v[16:19]
	v_mfma_f32_16x16x32_bf16 v[8:11], v[162:165], v[218:221], v[8:11]
	v_mfma_f32_16x16x32_bf16 v[0:3], v[186:189], v[218:221], v[0:3]
	v_mfma_f32_16x16x32_bf16 v[56:59], v[182:185], v[198:201], v[56:59]
	v_mfma_f32_16x16x32_bf16 v[48:51], v[190:193], v[198:201], v[48:51]
	v_mfma_f32_16x16x32_bf16 v[40:43], v[182:185], v[206:209], v[40:43]
	v_mfma_f32_16x16x32_bf16 v[32:35], v[190:193], v[206:209], v[32:35]
	v_mfma_f32_16x16x32_bf16 v[24:27], v[182:185], v[214:217], v[24:27]
	v_mfma_f32_16x16x32_bf16 v[16:19], v[190:193], v[214:217], v[16:19]
	v_mfma_f32_16x16x32_bf16 v[8:11], v[182:185], v[222:225], v[8:11]
	v_mfma_f32_16x16x32_bf16 v[0:3], v[190:193], v[222:225], v[0:3]
	s_barrier
	s_setprio 0
	s_add_i32 s62, s62, 2
	s_add_u32 s16, s16, 0x10000
	s_addc_u32 s17, s17, 0
	s_add_u32 s60, s60, 0x10000
	s_addc_u32 s61, s61, 0

; #define PG8_STAGE(bufoff, gbase, voff) do { _Pragma("unroll") for (int _i = 0; _i < 2; ++_i) \
;         __builtin_amdgcn_global_load_lds((const unsigned*)((const char*)(gbase) + (voff)[_i]), (PG8_LAS unsigned*)(lds + (bufoff) + ldsw + _i * 8192), 16, 0, 0); } while (0)
; #define PG8_LDA(dst, b, h) do { _Pragma("unroll") for (int m = 0; m < 4; ++m) _Pragma("unroll") for (int k = 0; k < 2; ++k) dst[m][k] = *(const PG8_LAS bf16x8*)(lds + PG8_SA(b, h) + aoff + m * 2048 + k * 1024); } while (0)
; #define PG8_LDB(dst, b, h) do { _Pragma("unroll") for (int n = 0; n < 2; ++n) _Pragma("unroll") for (int k = 0; k < 2; ++k) dst[n][k] = *(const PG8_LAS bf16x8*)(lds + PG8_SB(b, h) + boff + n * 2048 + k * 1024); } while (0)
; #define PG8_WAIT_V(n) asm volatile("s_waitcnt vmcnt(" #n ")" ::: "memory")
; #define PG8_WAIT_L(n) asm volatile("s_waitcnt lgkmcnt(" #n ")" ::: "memory")
; #define PG8_BAR __builtin_amdgcn_s_barrier()
; #define PG8_SCHED __builtin_amdgcn_sched_barrier(0)
; template <class Epi, class Sched, bool ALIGN_EPI>
; __device__ __forceinline__ void gemm_phase(PG8_LAS unsigned char* lds, const Gemm g, const Sched& S, const Epi& E, const int tid) {
;     ...
;         const bool has_next = S.next(ui + 1, nxt);
;         const char* nA = has_next ? (const char*)g.A + (size_t)nxt.pm * tstepA + PG8_ACOL(nxt) : cA; const char* nB = has_next ? (const char*)g.Bt + (size_t)nxt.pn * tstepB : cB;
;         for (int t = 0; t < nt; t += 2) {
;             const bool last = (t == nt - 2);
;             const char* a1 = cA + (size_t)(t + 1) * kstepA;
;             const char* a2 = last ? nA : cA + (size_t)(t + 2) * kstepA; const char* b2 = last ? nB : cB + (size_t)(t + 2) * kstepB;
;             const char* a3 = a2 + kstepA; const char* b3 = b2 + kstepB;
;             if (last && has_next) S.a_ready(nxt);
;             PG8_LDB(B0, 0, 0); PG8_LDB(B1, 0, 1); PG8_SCHED; PG8_LDA(At, 0, 0); PG8_STAGE(PG8_SA(1, 1), a1 + hstepA, voffA);
;             PG8_WAIT_V(8); PG8_WAIT_L(0); PG8_BAR; PG8_MMA(0, 0, At, B0); PG8_MMA(0, 1, At, B1); PG8_BAR; PG8_SCHED;
;             PG8_LDA(At, 0, 1); PG8_STAGE(PG8_SB(0, 0), b2, voffB); PG8_STAGE(PG8_SB(0, 1), b2 + hstepB, voffB); PG8_STAGE(PG8_SA(0, 0), a2, voffA);
;             PG8_WAIT_V(8); PG8_WAIT_L(0); PG8_BAR; PG8_MMA(1, 0, At, B0); PG8_MMA(1, 1, At, B1); PG8_BAR; PG8_SCHED;
.LBB0_1395:
	s_add_u32 s50, s18, s68
	s_addc_u32 s51, s19, s69
	s_add_u32 s52, s20, 0x10000
	s_addc_u32 s53, s21, 0
	s_mov_b64 s[20:21], 0
	v_add_u32_e32 v192, 0x10000, v195
	s_add_u32 s54, s20, 1
	s_addc_u32 s55, s21, 0
	s_add_u32 s22, s20, 2
	s_addc_u32 s23, s21, 0
	s_lshl_b64 s[24:25], s[22:23], s44
	s_add_u32 s21, s18, s24
	s_addc_u32 s24, s19, s25
	s_cmp_eq_u32 s45, s20
	s_cselect_b32 s26, s8, s21
	s_cselect_b32 s27, s9, s24
	s_cselect_b32 s24, s16, s52
	s_cselect_b32 s25, s17, s53
	s_add_u32 s20, s26, s38
	s_addc_u32 s21, s27, 0
	s_add_i32 s56, 0, 0x10000
	s_add_i32 s57, 0, 0x14000
	ds_read_b128 v[88:91], v192
	ds_read_b128 v[92:95], v192 offset:1024
	ds_read_b128 v[100:103], v192 offset:2048
	ds_read_b128 v[108:111], v192 offset:3072
	ds_read_b128 v[146:149], v192 offset:16384
	ds_read_b128 v[150:153], v192 offset:17408
	ds_read_b128 v[154:157], v192 offset:18432
	ds_read_b128 v[158:161], v192 offset:19456
	s_lshl_b64 s[54:55], s[54:55], s44
	s_add_u32 s54, s50, s54
	s_addc_u32 s55, s51, s55
	s_add_i32 m0, s31, 0xc000
	ds_read_b128 v[162:165], v185
	ds_read_b128 v[166:169], v185 offset:1024
	ds_read_b128 v[172:175], v185 offset:2048
	ds_read_b128 v[188:191], v185 offset:3072
	ds_read_b128 v[196:199], v185 offset:4096
	ds_read_b128 v[200:203], v185 offset:5120
	ds_read_b128 v[204:207], v185 offset:6144
	ds_read_b128 v[208:211], v185 offset:7168
	global_load_lds_dwordx4 v176, s[54:55]
	s_add_i32 m0, s31, 0xe000
	s_nop 0
	global_load_lds_dwordx4 v180, s[54:55]
	s_waitcnt vmcnt(8)
	s_waitcnt lgkmcnt(0)
	s_setprio 1
	s_barrier
	v_mfma_f32_16x16x32_bf16 v[142:145], v[88:91], v[162:165], 0
	v_mfma_f32_16x16x32_bf16 v[138:141], v[100:103], v[162:165], 0
	v_mfma_f32_16x16x32_bf16 v[124:127], v[88:91], v[172:175], 0
	v_mfma_f32_16x16x32_bf16 v[120:123], v[100:103], v[172:175], 0
	v_mfma_f32_16x16x32_bf16 v[104:107], v[88:91], v[196:199], 0
	v_mfma_f32_16x16x32_bf16 v[96:99], v[100:103], v[196:199], 0
	v_mfma_f32_16x16x32_bf16 v[76:79], v[88:91], v[204:207], 0
	v_mfma_f32_16x16x32_bf16 v[72:75], v[100:103], v[204:207], 0
	v_mfma_f32_16x16x32_bf16 v[142:145], v[92:95], v[166:169], v[142:145]
	v_mfma_f32_16x16x32_bf16 v[138:141], v[108:111], v[166:169], v[138:141]
	v_mfma_f32_16x16x32_bf16 v[124:127], v[92:95], v[188:191], v[124:127]
	v_mfma_f32_16x16x32_bf16 v[120:123], v[108:111], v[188:191], v[120:123]
	v_mfma_f32_16x16x32_bf16 v[104:107], v[92:95], v[200:203], v[104:107]
	v_mfma_f32_16x16x32_bf16 v[96:99], v[108:111], v[200:203], v[96:99]
	v_mfma_f32_16x16x32_bf16 v[76:79], v[92:95], v[208:211], v[76:79]
	v_mfma_f32_16x16x32_bf16 v[72:75], v[108:111], v[208:211], v[72:75]
	v_mfma_f32_16x16x32_bf16 v[134:137], v[146:149], v[162:165], 0
	v_mfma_f32_16x16x32_bf16 v[130:133], v[154:157], v[162:165], 0
	v_mfma_f32_16x16x32_bf16 v[116:119], v[146:149], v[172:175], 0
	v_mfma_f32_16x16x32_bf16 v[112:115], v[154:157], v[172:175], 0
	v_mfma_f32_16x16x32_bf16 v[84:87], v[146:149], v[196:199], 0
	v_mfma_f32_16x16x32_bf16 v[80:83], v[154:157], v[196:199], 0
	v_mfma_f32_16x16x32_bf16 v[68:71], v[146:149], v[204:207], 0
	v_mfma_f32_16x16x32_bf16 v[64:67], v[154:157], v[204:207], 0
	v_mfma_f32_16x16x32_bf16 v[134:137], v[150:153], v[166:169], v[134:137]
	v_mfma_f32_16x16x32_bf16 v[130:133], v[158:161], v[166:169], v[130:133]
	v_mfma_f32_16x16x32_bf16 v[116:119], v[150:153], v[188:191], v[116:119]
	v_mfma_f32_16x16x32_bf16 v[112:115], v[158:161], v[188:191], v[112:115]
	v_mfma_f32_16x16x32_bf16 v[84:87], v[150:153], v[200:203], v[84:87]
	v_mfma_f32_16x16x32_bf16 v[80:83], v[158:161], v[200:203], v[80:83]
	v_mfma_f32_16x16x32_bf16 v[68:71], v[150:153], v[208:211], v[68:71]
	v_mfma_f32_16x16x32_bf16 v[64:67], v[158:161], v[208:211], v[64:67]
	s_barrier
	s_setprio 0
	s_add_i32 s54, s56, s30
	s_mov_b32 m0, s54
	ds_read_b128 v[162:165], v185 offset:16384
	ds_read_b128 v[166:169], v185 offset:17408
	ds_read_b128 v[172:175], v185 offset:18432
	ds_read_b128 v[188:191], v185 offset:19456
	ds_read_b128 v[196:199], v185 offset:20480
	ds_read_b128 v[200:203], v185 offset:21504
	ds_read_b128 v[204:207], v185 offset:22528
	ds_read_b128 v[208:211], v185 offset:23552
	global_load_lds_dwordx4 v178, s[24:25]
	s_add_i32 m0, s54, 0x2000
	s_add_u32 s54, s24, 0x4000
	s_addc_u32 s55, s25, 0
	s_add_i32 s56, s57, s30
	global_load_lds_dwordx4 v182, s[24:25]
	s_mov_b32 m0, s56
	s_nop 0
	global_load_lds_dwordx4 v178, s[54:55]
	s_add_i32 m0, s56, 0x2000
	s_nop 0
	global_load_lds_dwordx4 v182, s[54:55]
	s_mov_b32 m0, s31
	s_nop 0
	global_load_lds_dwordx4 v176, s[26:27]
	s_mov_b32 m0, s33
	s_nop 0
	global_load_lds_dwordx4 v180, s[26:27]
	s_waitcnt vmcnt(8)
	s_waitcnt lgkmcnt(0)
	s_setprio 1
	s_barrier
; #define PG8_STAGE(bufoff, gbase, voff) do { _Pragma("unroll") for (int _i = 0; _i < 2; ++_i) \
;         __builtin_amdgcn_global_load_lds((const unsigned*)((const char*)(gbase) + (voff)[_i]), (PG8_LAS unsigned*)(lds + (bufoff) + ldsw + _i * 8192), 16, 0, 0); } while (0)
; #define PG8_LDA(dst, b, h) do { _Pragma("unroll") for (int m = 0; m < 4; ++m) _Pragma("unroll") for (int k = 0; k < 2; ++k) dst[m][k] = *(const PG8_LAS bf16x8*)(lds + PG8_SA(b, h) + aoff + m * 2048 + k * 1024); } while (0)
; #define PG8_LDB(dst, b, h) do { _Pragma("unroll") for (int n = 0; n < 2; ++n) _Pragma("unroll") for (int k = 0; k < 2; ++k) dst[n][k] = *(const PG8_LAS bf16x8*)(lds + PG8_SB(b, h) + boff + n * 2048 + k * 1024); } while (0)
; #define PG8_MMA(ai, bj, At, Bt) do { __builtin_amdgcn_s_setprio(1); _Pragma("unroll") for (int m = 0; m < 4; ++m) _Pragma("unroll") for (int n = 0; n < 2; ++n) _Pragma("unroll") for (int k = 0; k < 2; ++k) \
;         acc[ai][bj][m][n] = __builtin_amdgcn_mfma_f32_16x16x32_bf16(Bt[n][k], At[m][k], acc[ai][bj][m][n], 0, 0, 0); __builtin_amdgcn_s_setprio(0); } while (0)
; #define PG8_WAIT_V(n) asm volatile("s_waitcnt vmcnt(" #n ")" ::: "memory")
; #define PG8_WAIT_L(n) asm volatile("s_waitcnt lgkmcnt(" #n ")" ::: "memory")
; #define PG8_BAR __builtin_amdgcn_s_barrier()
; #define PG8_SCHED __builtin_amdgcn_sched_barrier(0)
; template <class Epi, class Sched, bool ALIGN_EPI>
; __device__ __forceinline__ void gemm_phase(PG8_LAS unsigned char* lds, const Gemm g, const Sched& S, const Epi& E, const int tid) {
;     ...
;             PG8_WAIT_V(8); PG8_WAIT_L(0); PG8_BAR; PG8_MMA(1, 0, At, B0); PG8_MMA(1, 1, At, B1); PG8_BAR; PG8_SCHED;
;             PG8_LDB(B0, 1, 0); PG8_LDB(B1, 1, 1); PG8_SCHED; PG8_LDA(At, 1, 0); PG8_STAGE(PG8_SA(0, 1), a2 + hstepA, voffA);
;             PG8_WAIT_V(8); PG8_WAIT_L(0); PG8_BAR; PG8_MMA(0, 0, At, B0); PG8_MMA(0, 1, At, B1); PG8_BAR; PG8_SCHED;
;             PG8_LDA(At, 1, 1); PG8_STAGE(PG8_SB(1, 0), b3, voffB); PG8_STAGE(PG8_SB(1, 1), b3 + hstepB, voffB); PG8_STAGE(PG8_SA(1, 0), a3, voffA);
	v_mfma_f32_16x16x32_bf16 v[60:63], v[88:91], v[162:165], 0
	v_mfma_f32_16x16x32_bf16 v[56:59], v[100:103], v[162:165], 0
	v_mfma_f32_16x16x32_bf16 v[44:47], v[88:91], v[172:175], 0
	v_mfma_f32_16x16x32_bf16 v[40:43], v[100:103], v[172:175], 0
	v_mfma_f32_16x16x32_bf16 v[28:31], v[88:91], v[196:199], 0
	v_mfma_f32_16x16x32_bf16 v[24:27], v[100:103], v[196:199], 0
	v_mfma_f32_16x16x32_bf16 v[12:15], v[88:91], v[204:207], 0
	v_mfma_f32_16x16x32_bf16 v[8:11], v[100:103], v[204:207], 0
	v_mfma_f32_16x16x32_bf16 v[60:63], v[92:95], v[166:169], v[60:63]
	v_mfma_f32_16x16x32_bf16 v[56:59], v[108:111], v[166:169], v[56:59]
	v_mfma_f32_16x16x32_bf16 v[44:47], v[92:95], v[188:191], v[44:47]
	v_mfma_f32_16x16x32_bf16 v[40:43], v[108:111], v[188:191], v[40:43]
	v_mfma_f32_16x16x32_bf16 v[28:31], v[92:95], v[200:203], v[28:31]
	v_mfma_f32_16x16x32_bf16 v[24:27], v[108:111], v[200:203], v[24:27]
	v_mfma_f32_16x16x32_bf16 v[12:15], v[92:95], v[208:211], v[12:15]
	v_mfma_f32_16x16x32_bf16 v[8:11], v[108:111], v[208:211], v[8:11]
	v_mfma_f32_16x16x32_bf16 v[52:55], v[146:149], v[162:165], 0
	v_mfma_f32_16x16x32_bf16 v[48:51], v[154:157], v[162:165], 0
	v_mfma_f32_16x16x32_bf16 v[36:39], v[146:149], v[172:175], 0
	v_mfma_f32_16x16x32_bf16 v[32:35], v[154:157], v[172:175], 0
	v_mfma_f32_16x16x32_bf16 v[20:23], v[146:149], v[196:199], 0
	v_mfma_f32_16x16x32_bf16 v[16:19], v[154:157], v[196:199], 0
	v_mfma_f32_16x16x32_bf16 v[4:7], v[146:149], v[204:207], 0
	v_mfma_f32_16x16x32_bf16 v[0:3], v[154:157], v[204:207], 0
	v_mfma_f32_16x16x32_bf16 v[52:55], v[150:153], v[166:169], v[52:55]
	v_mfma_f32_16x16x32_bf16 v[48:51], v[158:161], v[166:169], v[48:51]
	v_mfma_f32_16x16x32_bf16 v[36:39], v[150:153], v[188:191], v[36:39]
	v_mfma_f32_16x16x32_bf16 v[32:35], v[158:161], v[188:191], v[32:35]
	v_mfma_f32_16x16x32_bf16 v[20:23], v[150:153], v[200:203], v[20:23]
	v_mfma_f32_16x16x32_bf16 v[16:19], v[158:161], v[200:203], v[16:19]
	v_mfma_f32_16x16x32_bf16 v[4:7], v[150:153], v[208:211], v[4:7]
	v_mfma_f32_16x16x32_bf16 v[0:3], v[158:161], v[208:211], v[0:3]
	s_barrier
	s_setprio 0
	s_add_i32 s54, 0, 0x18000
	s_add_i32 s55, 0, 0x1c000
	ds_read_b128 v[88:91], v192 offset:32768
	ds_read_b128 v[92:95], v192 offset:33792
	ds_read_b128 v[100:103], v192 offset:34816
	ds_read_b128 v[108:111], v192 offset:35840
	ds_read_b128 v[146:149], v192 offset:49152
	ds_read_b128 v[150:153], v192 offset:50176
	ds_read_b128 v[154:157], v192 offset:51200
	ds_read_b128 v[158:161], v192 offset:52224
	s_add_u32 s26, s26, s68
	s_addc_u32 s27, s27, s69
	s_mov_b32 m0, s34
	ds_read_b128 v[162:165], v185 offset:32768
	ds_read_b128 v[166:169], v185 offset:33792
	ds_read_b128 v[172:175], v185 offset:34816
	ds_read_b128 v[188:191], v185 offset:35840
	ds_read_b128 v[196:199], v185 offset:36864
	ds_read_b128 v[200:203], v185 offset:37888
	ds_read_b128 v[204:207], v185 offset:38912
	ds_read_b128 v[208:211], v185 offset:39936
	global_load_lds_dwordx4 v176, s[26:27]
	s_mov_b32 m0, s35
	s_nop 0
	global_load_lds_dwordx4 v180, s[26:27]
	s_waitcnt vmcnt(8)
	s_waitcnt lgkmcnt(0)
	s_setprio 1
	s_barrier
	v_mfma_f32_16x16x32_bf16 v[142:145], v[88:91], v[162:165], v[142:145]
	v_mfma_f32_16x16x32_bf16 v[138:141], v[100:103], v[162:165], v[138:141]
	v_mfma_f32_16x16x32_bf16 v[124:127], v[88:91], v[172:175], v[124:127]
	v_mfma_f32_16x16x32_bf16 v[120:123], v[100:103], v[172:175], v[120:123]
	v_mfma_f32_16x16x32_bf16 v[104:107], v[88:91], v[196:199], v[104:107]
	v_mfma_f32_16x16x32_bf16 v[96:99], v[100:103], v[196:199], v[96:99]
	v_mfma_f32_16x16x32_bf16 v[76:79], v[88:91], v[204:207], v[76:79]
	v_mfma_f32_16x16x32_bf16 v[72:75], v[100:103], v[204:207], v[72:75]
	v_mfma_f32_16x16x32_bf16 v[142:145], v[92:95], v[166:169], v[142:145]
	v_mfma_f32_16x16x32_bf16 v[138:141], v[108:111], v[166:169], v[138:141]
	v_mfma_f32_16x16x32_bf16 v[124:127], v[92:95], v[188:191], v[124:127]
	v_mfma_f32_16x16x32_bf16 v[120:123], v[108:111], v[188:191], v[120:123]
	v_mfma_f32_16x16x32_bf16 v[104:107], v[92:95], v[200:203], v[104:107]
	v_mfma_f32_16x16x32_bf16 v[96:99], v[108:111], v[200:203], v[96:99]
	v_mfma_f32_16x16x32_bf16 v[76:79], v[92:95], v[208:211], v[76:79]
	v_mfma_f32_16x16x32_bf16 v[72:75], v[108:111], v[208:211], v[72:75]
	v_mfma_f32_16x16x32_bf16 v[134:137], v[146:149], v[162:165], v[134:137]
	v_mfma_f32_16x16x32_bf16 v[130:133], v[154:157], v[162:165], v[130:133]
	v_mfma_f32_16x16x32_bf16 v[116:119], v[146:149], v[172:175], v[116:119]
	v_mfma_f32_16x16x32_bf16 v[112:115], v[154:157], v[172:175], v[112:115]
	v_mfma_f32_16x16x32_bf16 v[84:87], v[146:149], v[196:199], v[84:87]
	v_mfma_f32_16x16x32_bf16 v[80:83], v[154:157], v[196:199], v[80:83]
	v_mfma_f32_16x16x32_bf16 v[68:71], v[146:149], v[204:207], v[68:71]
	v_mfma_f32_16x16x32_bf16 v[64:67], v[154:157], v[204:207], v[64:67]
	v_mfma_f32_16x16x32_bf16 v[134:137], v[150:153], v[166:169], v[134:137]
	v_mfma_f32_16x16x32_bf16 v[130:133], v[158:161], v[166:169], v[130:133]
	v_mfma_f32_16x16x32_bf16 v[116:119], v[150:153], v[188:191], v[116:119]
	v_mfma_f32_16x16x32_bf16 v[112:115], v[158:161], v[188:191], v[112:115]
	v_mfma_f32_16x16x32_bf16 v[84:87], v[150:153], v[200:203], v[84:87]
	v_mfma_f32_16x16x32_bf16 v[80:83], v[158:161], v[200:203], v[80:83]
	v_mfma_f32_16x16x32_bf16 v[68:71], v[150:153], v[208:211], v[68:71]
	v_mfma_f32_16x16x32_bf16 v[64:67], v[158:161], v[208:211], v[64:67]
	s_barrier
; #define PG8_STAGE(bufoff, gbase, voff) do { _Pragma("unroll") for (int _i = 0; _i < 2; ++_i) \
;         __builtin_amdgcn_global_load_lds((const unsigned*)((const char*)(gbase) + (voff)[_i]), (PG8_LAS unsigned*)(lds + (bufoff) + ldsw + _i * 8192), 16, 0, 0); } while (0)
; #define PG8_LDA(dst, b, h) do { _Pragma("unroll") for (int m = 0; m < 4; ++m) _Pragma("unroll") for (int k = 0; k < 2; ++k) dst[m][k] = *(const PG8_LAS bf16x8*)(lds + PG8_SA(b, h) + aoff + m * 2048 + k * 1024); } while (0)
; #define PG8_MMA(ai, bj, At, Bt) do { __builtin_amdgcn_s_setprio(1); _Pragma("unroll") for (int m = 0; m < 4; ++m) _Pragma("unroll") for (int n = 0; n < 2; ++n) _Pragma("unroll") for (int k = 0; k < 2; ++k) \
;         acc[ai][bj][m][n] = __builtin_amdgcn_mfma_f32_16x16x32_bf16(Bt[n][k], At[m][k], acc[ai][bj][m][n], 0, 0, 0); __builtin_amdgcn_s_setprio(0); } while (0)
; #define PG8_WAIT_V(n) asm volatile("s_waitcnt vmcnt(" #n ")" ::: "memory")
; #define PG8_WAIT_L(n) asm volatile("s_waitcnt lgkmcnt(" #n ")" ::: "memory")
; #define PG8_BAR __builtin_amdgcn_s_barrier()
; #define PG8_SCHED __builtin_amdgcn_sched_barrier(0)
; template <class Epi, class Sched, bool ALIGN_EPI>
; __device__ __forceinline__ void gemm_phase(PG8_LAS unsigned char* lds, const Gemm g, const Sched& S, const Epi& E, const int tid) {
;     ...
;             PG8_LDA(At, 1, 1); PG8_STAGE(PG8_SB(1, 0), b3, voffB); PG8_STAGE(PG8_SB(1, 1), b3 + hstepB, voffB); PG8_STAGE(PG8_SA(1, 0), a3, voffA);
;             PG8_WAIT_V(8); PG8_WAIT_L(0); PG8_BAR; PG8_MMA(1, 0, At, B0); PG8_MMA(1, 1, At, B1); PG8_BAR; PG8_SCHED;
;         }
	s_setprio 0
	s_add_u32 s26, s24, 0x8000
	s_addc_u32 s27, s25, 0
	s_add_i32 s54, s54, s30
	s_mov_b32 m0, s54
	ds_read_b128 v[162:165], v185 offset:49152
	ds_read_b128 v[166:169], v185 offset:50176
	ds_read_b128 v[172:175], v185 offset:51200
	ds_read_b128 v[188:191], v185 offset:52224
	ds_read_b128 v[196:199], v185 offset:53248
	ds_read_b128 v[200:203], v185 offset:54272
	ds_read_b128 v[204:207], v185 offset:55296
	ds_read_b128 v[208:211], v185 offset:56320
	global_load_lds_dwordx4 v178, s[26:27]
	s_add_i32 m0, s54, 0x2000
	s_add_u32 s24, s24, 0xc000
	s_addc_u32 s25, s25, 0
	global_load_lds_dwordx4 v182, s[26:27]
	s_add_i32 s26, s55, s30
	s_mov_b32 m0, s26
	s_nop 0
	global_load_lds_dwordx4 v178, s[24:25]
	s_add_i32 m0, s26, 0x2000
	s_nop 0
	global_load_lds_dwordx4 v182, s[24:25]
	s_mov_b32 m0, s40
	s_nop 0
	global_load_lds_dwordx4 v176, s[20:21]
	s_mov_b32 m0, s41
	s_nop 0
	global_load_lds_dwordx4 v180, s[20:21]
	s_waitcnt vmcnt(8)
	s_waitcnt lgkmcnt(0)
	s_setprio 1
	s_barrier
	v_mfma_f32_16x16x32_bf16 v[60:63], v[88:91], v[162:165], v[60:63]
	v_mfma_f32_16x16x32_bf16 v[56:59], v[100:103], v[162:165], v[56:59]
	v_mfma_f32_16x16x32_bf16 v[44:47], v[88:91], v[172:175], v[44:47]
	v_mfma_f32_16x16x32_bf16 v[40:43], v[100:103], v[172:175], v[40:43]
	v_mfma_f32_16x16x32_bf16 v[28:31], v[88:91], v[196:199], v[28:31]
	v_mfma_f32_16x16x32_bf16 v[24:27], v[100:103], v[196:199], v[24:27]
	v_mfma_f32_16x16x32_bf16 v[12:15], v[88:91], v[204:207], v[12:15]
	v_mfma_f32_16x16x32_bf16 v[8:11], v[100:103], v[204:207], v[8:11]
	v_mfma_f32_16x16x32_bf16 v[60:63], v[92:95], v[166:169], v[60:63]
	v_mfma_f32_16x16x32_bf16 v[56:59], v[108:111], v[166:169], v[56:59]
	v_mfma_f32_16x16x32_bf16 v[44:47], v[92:95], v[188:191], v[44:47]
	v_mfma_f32_16x16x32_bf16 v[40:43], v[108:111], v[188:191], v[40:43]
	v_mfma_f32_16x16x32_bf16 v[28:31], v[92:95], v[200:203], v[28:31]
	v_mfma_f32_16x16x32_bf16 v[24:27], v[108:111], v[200:203], v[24:27]
	v_mfma_f32_16x16x32_bf16 v[12:15], v[92:95], v[208:211], v[12:15]
	v_mfma_f32_16x16x32_bf16 v[8:11], v[108:111], v[208:211], v[8:11]
	v_mfma_f32_16x16x32_bf16 v[52:55], v[146:149], v[162:165], v[52:55]
	v_mfma_f32_16x16x32_bf16 v[48:51], v[154:157], v[162:165], v[48:51]
	v_mfma_f32_16x16x32_bf16 v[36:39], v[146:149], v[172:175], v[36:39]
	v_mfma_f32_16x16x32_bf16 v[32:35], v[154:157], v[172:175], v[32:35]
	v_mfma_f32_16x16x32_bf16 v[20:23], v[146:149], v[196:199], v[20:23]
	v_mfma_f32_16x16x32_bf16 v[16:19], v[154:157], v[196:199], v[16:19]
	v_mfma_f32_16x16x32_bf16 v[4:7], v[146:149], v[204:207], v[4:7]
	v_mfma_f32_16x16x32_bf16 v[0:3], v[154:157], v[204:207], v[0:3]
	v_mfma_f32_16x16x32_bf16 v[52:55], v[150:153], v[166:169], v[52:55]
	v_mfma_f32_16x16x32_bf16 v[48:51], v[158:161], v[166:169], v[48:51]
	v_mfma_f32_16x16x32_bf16 v[36:39], v[150:153], v[188:191], v[36:39]
	v_mfma_f32_16x16x32_bf16 v[32:35], v[158:161], v[188:191], v[32:35]
	v_mfma_f32_16x16x32_bf16 v[20:23], v[150:153], v[200:203], v[20:23]
	v_mfma_f32_16x16x32_bf16 v[16:19], v[158:161], v[200:203], v[16:19]
	v_mfma_f32_16x16x32_bf16 v[4:7], v[150:153], v[208:211], v[4:7]
	v_mfma_f32_16x16x32_bf16 v[0:3], v[158:161], v[208:211], v[0:3]
	s_barrier
	s_setprio 0
	s_add_u32 s52, s52, 0x10000
	s_addc_u32 s53, s53, 0
	s_mov_b64 s[20:21], s[22:23]
